# MoE1 swiglu epilogue regenerated: packed f32 ops, the two exp-argument constant multiplies merged, (x+1)*4 as one fma; on top of the nt cache hints
# speedup vs baseline: 1.0200x; 1.0043x over previous
.LBB0_2077:
	v_lshl_or_b32 v20, s53, 7, v219
	s_ashr_i32 s53, s52, 31
	s_lshl_b64 s[52:53], s[52:53], 14
	s_add_u32 s52, s40, s52
	s_addc_u32 s53, s41, s53
	v_ashrrev_i32_e32 v21, 31, v20
	v_lshl_add_u64 v[2:3], v[20:21], 2, s[52:53]
	s_nop 15
	s_nop 15
	s_nop 15
	s_nop 15
	global_load_dwordx4 v[14:17], v[2:3], off
	global_load_dwordx4 v[6:9], v[2:3], off offset:16
	v_add_co_u32_e32 v4, vcc, s76, v2
	v_lshl_add_u32 v22, s83, 8, v217
	s_nop 0
	v_addc_co_u32_e32 v5, vcc, 0, v3, vcc
	global_load_dwordx4 v[10:13], v[4:5], off
	v_lshl_add_u64 v[2:3], v[2:3], 0, s[42:43]
	global_load_dwordx4 v[2:5], v[2:3], off offset:16
	s_waitcnt vmcnt(0)
	s_mov_b32 s90, 0x3c800000
	s_mov_b32 s92, 0xc01d265f
	s_mov_b32 s94, 0x3fb8aa3b
	s_mov_b32 s96, 1.0
	v_pk_fma_f32 v[238:239], v[190:191], s[90:91], v[14:15] op_sel_hi:[1,0,1]
	v_pk_fma_f32 v[240:241], v[192:193], s[90:91], v[16:17] op_sel_hi:[1,0,1]
	v_pk_fma_f32 v[242:243], v[182:183], s[90:91], v[6:7] op_sel_hi:[1,0,1]
	v_pk_fma_f32 v[244:245], v[184:185], s[90:91], v[8:9] op_sel_hi:[1,0,1]
	v_min_f32_e32 v238, 0x40e00000, v238
	v_min_f32_e32 v239, 0x40e00000, v239
	v_min_f32_e32 v240, 0x40e00000, v240
	v_min_f32_e32 v241, 0x40e00000, v241
	v_min_f32_e32 v242, 0x40e00000, v242
	v_min_f32_e32 v243, 0x40e00000, v243
	v_min_f32_e32 v244, 0x40e00000, v244
	v_min_f32_e32 v245, 0x40e00000, v245
	v_pk_mul_f32 v[246:247], v[238:239], s[92:93] op_sel_hi:[1,0]
	v_pk_mul_f32 v[248:249], v[240:241], s[92:93] op_sel_hi:[1,0]
	v_pk_mul_f32 v[250:251], v[242:243], s[92:93] op_sel_hi:[1,0]
	v_pk_mul_f32 v[252:253], v[244:245], s[92:93] op_sel_hi:[1,0]
	v_exp_f32_e32 v246, v246
	v_exp_f32_e32 v247, v247
	v_exp_f32_e32 v248, v248
	v_exp_f32_e32 v249, v249
	v_exp_f32_e32 v250, v250
	v_exp_f32_e32 v251, v251
	v_exp_f32_e32 v252, v252
	v_exp_f32_e32 v253, v253
	v_pk_add_f32 v[246:247], v[246:247], s[96:97] op_sel_hi:[1,0]
	v_pk_add_f32 v[248:249], v[248:249], s[96:97] op_sel_hi:[1,0]
	v_pk_add_f32 v[250:251], v[250:251], s[96:97] op_sel_hi:[1,0]
	v_pk_add_f32 v[252:253], v[252:253], s[96:97] op_sel_hi:[1,0]
	v_rcp_f32_e32 v246, v246
	v_rcp_f32_e32 v247, v247
	v_rcp_f32_e32 v248, v248
	v_rcp_f32_e32 v249, v249
	v_rcp_f32_e32 v250, v250
	v_rcp_f32_e32 v251, v251
	v_rcp_f32_e32 v252, v252
	v_rcp_f32_e32 v253, v253
	v_pk_mul_f32 v[238:239], v[238:239], v[246:247]
	v_pk_mul_f32 v[240:241], v[240:241], v[248:249]
	v_pk_mul_f32 v[242:243], v[242:243], v[250:251]
	v_pk_mul_f32 v[244:245], v[244:245], v[252:253]
	v_pk_fma_f32 v[246:247], v[186:187], s[90:91], v[10:11] op_sel_hi:[1,0,1]
	v_pk_fma_f32 v[248:249], v[188:189], s[90:91], v[12:13] op_sel_hi:[1,0,1]
	v_pk_fma_f32 v[250:251], v[178:179], s[90:91], v[2:3] op_sel_hi:[1,0,1]
	v_pk_fma_f32 v[252:253], v[180:181], s[90:91], v[4:5] op_sel_hi:[1,0,1]
	v_med3_f32 v246, v246, s79, v224
	v_med3_f32 v247, v247, s79, v224
	v_med3_f32 v248, v248, s79, v224
	v_med3_f32 v249, v249, s79, v224
	v_med3_f32 v250, v250, s79, v224
	v_med3_f32 v251, v251, s79, v224
	v_med3_f32 v252, v252, s79, v224
	v_med3_f32 v253, v253, s79, v224
	v_fma_f32 v246, v246, 4.0, 4.0
	v_fma_f32 v247, v247, 4.0, 4.0
	v_fma_f32 v248, v248, 4.0, 4.0
	v_fma_f32 v249, v249, 4.0, 4.0
	v_fma_f32 v250, v250, 4.0, 4.0
	v_fma_f32 v251, v251, 4.0, 4.0
	v_fma_f32 v252, v252, 4.0, 4.0
	v_fma_f32 v253, v253, 4.0, 4.0
	v_pk_mul_f32 v[238:239], v[246:247], v[238:239]
	v_pk_mul_f32 v[240:241], v[248:249], v[240:241]
	v_pk_mul_f32 v[242:243], v[250:251], v[242:243]
	v_pk_mul_f32 v[244:245], v[252:253], v[244:245]
	v_ashrrev_i32_e32 v23, 31, v22
	v_lshlrev_b64 v[18:19], 11, v[22:23]
	v_lshl_add_u64 v[18:19], s[6:7], 0, v[18:19]
	v_lshl_add_u64 v[18:19], v[18:19], 0, v[20:21]
	v_mov_b32_e32 v24, v201
	v_mov_b32_e32 v25, v201
	v_cvt_pk_fp8_f32 v24, v238, v239
	v_cvt_pk_fp8_f32 v25, v242, v243
	v_cvt_pk_fp8_f32 v24, v240, v241 op_sel:[0,0,1]
	v_cvt_pk_fp8_f32 v25, v244, v245 op_sel:[0,0,1]
	global_store_dwordx2 v[18:19], v[24:25], off
	v_pk_fma_f32 v[238:239], v[174:175], s[90:91], v[14:15] op_sel_hi:[1,0,1]
	v_pk_fma_f32 v[240:241], v[176:177], s[90:91], v[16:17] op_sel_hi:[1,0,1]
	v_pk_fma_f32 v[242:243], v[166:167], s[90:91], v[6:7] op_sel_hi:[1,0,1]
	v_pk_fma_f32 v[244:245], v[168:169], s[90:91], v[8:9] op_sel_hi:[1,0,1]
	v_min_f32_e32 v238, 0x40e00000, v238
	v_min_f32_e32 v239, 0x40e00000, v239
	v_min_f32_e32 v240, 0x40e00000, v240
	v_min_f32_e32 v241, 0x40e00000, v241
	v_min_f32_e32 v242, 0x40e00000, v242
	v_min_f32_e32 v243, 0x40e00000, v243
	v_min_f32_e32 v244, 0x40e00000, v244
	v_min_f32_e32 v245, 0x40e00000, v245
	v_pk_mul_f32 v[246:247], v[238:239], s[92:93] op_sel_hi:[1,0]
	v_pk_mul_f32 v[248:249], v[240:241], s[92:93] op_sel_hi:[1,0]
	v_pk_mul_f32 v[250:251], v[242:243], s[92:93] op_sel_hi:[1,0]
	v_pk_mul_f32 v[252:253], v[244:245], s[92:93] op_sel_hi:[1,0]
	v_exp_f32_e32 v246, v246
	v_exp_f32_e32 v247, v247
	v_exp_f32_e32 v248, v248
	v_exp_f32_e32 v249, v249
	v_exp_f32_e32 v250, v250
	v_exp_f32_e32 v251, v251
	v_exp_f32_e32 v252, v252
	v_exp_f32_e32 v253, v253
	v_pk_add_f32 v[246:247], v[246:247], s[96:97] op_sel_hi:[1,0]
	v_pk_add_f32 v[248:249], v[248:249], s[96:97] op_sel_hi:[1,0]
	v_pk_add_f32 v[250:251], v[250:251], s[96:97] op_sel_hi:[1,0]
	v_pk_add_f32 v[252:253], v[252:253], s[96:97] op_sel_hi:[1,0]
	v_rcp_f32_e32 v246, v246
	v_rcp_f32_e32 v247, v247
	v_rcp_f32_e32 v248, v248
	v_rcp_f32_e32 v249, v249
	v_rcp_f32_e32 v250, v250
	v_rcp_f32_e32 v251, v251
	v_rcp_f32_e32 v252, v252
	v_rcp_f32_e32 v253, v253
	v_pk_mul_f32 v[238:239], v[238:239], v[246:247]
	v_pk_mul_f32 v[240:241], v[240:241], v[248:249]
	v_pk_mul_f32 v[242:243], v[242:243], v[250:251]
	v_pk_mul_f32 v[244:245], v[244:245], v[252:253]
	v_pk_fma_f32 v[246:247], v[170:171], s[90:91], v[10:11] op_sel_hi:[1,0,1]
	v_pk_fma_f32 v[248:249], v[172:173], s[90:91], v[12:13] op_sel_hi:[1,0,1]
	v_pk_fma_f32 v[250:251], v[162:163], s[90:91], v[2:3] op_sel_hi:[1,0,1]
	v_pk_fma_f32 v[252:253], v[164:165], s[90:91], v[4:5] op_sel_hi:[1,0,1]
	v_med3_f32 v246, v246, s79, v224
	v_med3_f32 v247, v247, s79, v224
	v_med3_f32 v248, v248, s79, v224
	v_med3_f32 v249, v249, s79, v224
	v_med3_f32 v250, v250, s79, v224
	v_med3_f32 v251, v251, s79, v224
	v_med3_f32 v252, v252, s79, v224
	v_med3_f32 v253, v253, s79, v224
	v_fma_f32 v246, v246, 4.0, 4.0
	v_fma_f32 v247, v247, 4.0, 4.0
	v_fma_f32 v248, v248, 4.0, 4.0
	v_fma_f32 v249, v249, 4.0, 4.0
	v_fma_f32 v250, v250, 4.0, 4.0
	v_fma_f32 v251, v251, 4.0, 4.0
	v_fma_f32 v252, v252, 4.0, 4.0
	v_fma_f32 v253, v253, 4.0, 4.0
	v_pk_mul_f32 v[238:239], v[246:247], v[238:239]
	v_pk_mul_f32 v[240:241], v[248:249], v[240:241]
	v_pk_mul_f32 v[242:243], v[250:251], v[242:243]
	v_pk_mul_f32 v[244:245], v[252:253], v[244:245]
	v_or_b32_e32 v26, 16, v22
	v_ashrrev_i32_e32 v27, 31, v26
	v_lshlrev_b64 v[26:27], 11, v[26:27]
	v_lshl_add_u64 v[26:27], s[6:7], 0, v[26:27]
	v_lshl_add_u64 v[26:27], v[26:27], 0, v[20:21]
	v_mov_b32_e32 v24, v201
	v_mov_b32_e32 v25, v201
	v_cvt_pk_fp8_f32 v24, v238, v239
	v_cvt_pk_fp8_f32 v25, v242, v243
	v_cvt_pk_fp8_f32 v24, v240, v241 op_sel:[0,0,1]
	v_cvt_pk_fp8_f32 v25, v244, v245 op_sel:[0,0,1]
	global_store_dwordx2 v[26:27], v[24:25], off
	v_pk_fma_f32 v[238:239], v[158:159], s[90:91], v[14:15] op_sel_hi:[1,0,1]
	v_pk_fma_f32 v[240:241], v[160:161], s[90:91], v[16:17] op_sel_hi:[1,0,1]
	v_pk_fma_f32 v[242:243], v[150:151], s[90:91], v[6:7] op_sel_hi:[1,0,1]
	v_pk_fma_f32 v[244:245], v[152:153], s[90:91], v[8:9] op_sel_hi:[1,0,1]
	v_min_f32_e32 v238, 0x40e00000, v238
	v_min_f32_e32 v239, 0x40e00000, v239
	v_min_f32_e32 v240, 0x40e00000, v240
	v_min_f32_e32 v241, 0x40e00000, v241
	v_min_f32_e32 v242, 0x40e00000, v242
	v_min_f32_e32 v243, 0x40e00000, v243
	v_min_f32_e32 v244, 0x40e00000, v244
	v_min_f32_e32 v245, 0x40e00000, v245
	v_pk_mul_f32 v[246:247], v[238:239], s[92:93] op_sel_hi:[1,0]
	v_pk_mul_f32 v[248:249], v[240:241], s[92:93] op_sel_hi:[1,0]
	v_pk_mul_f32 v[250:251], v[242:243], s[92:93] op_sel_hi:[1,0]
	v_pk_mul_f32 v[252:253], v[244:245], s[92:93] op_sel_hi:[1,0]
	v_exp_f32_e32 v246, v246
	v_exp_f32_e32 v247, v247
	v_exp_f32_e32 v248, v248
	v_exp_f32_e32 v249, v249
	v_exp_f32_e32 v250, v250
	v_exp_f32_e32 v251, v251
	v_exp_f32_e32 v252, v252
	v_exp_f32_e32 v253, v253
	v_pk_add_f32 v[246:247], v[246:247], s[96:97] op_sel_hi:[1,0]
	v_pk_add_f32 v[248:249], v[248:249], s[96:97] op_sel_hi:[1,0]
	v_pk_add_f32 v[250:251], v[250:251], s[96:97] op_sel_hi:[1,0]
	v_pk_add_f32 v[252:253], v[252:253], s[96:97] op_sel_hi:[1,0]
	v_rcp_f32_e32 v246, v246
	v_rcp_f32_e32 v247, v247
	v_rcp_f32_e32 v248, v248
	v_rcp_f32_e32 v249, v249
	v_rcp_f32_e32 v250, v250
	v_rcp_f32_e32 v251, v251
	v_rcp_f32_e32 v252, v252
	v_rcp_f32_e32 v253, v253
	v_pk_mul_f32 v[238:239], v[238:239], v[246:247]
	v_pk_mul_f32 v[240:241], v[240:241], v[248:249]
	v_pk_mul_f32 v[242:243], v[242:243], v[250:251]
	v_pk_mul_f32 v[244:245], v[244:245], v[252:253]
	v_pk_fma_f32 v[246:247], v[154:155], s[90:91], v[10:11] op_sel_hi:[1,0,1]
	v_pk_fma_f32 v[248:249], v[156:157], s[90:91], v[12:13] op_sel_hi:[1,0,1]
	v_pk_fma_f32 v[250:251], v[146:147], s[90:91], v[2:3] op_sel_hi:[1,0,1]
	v_pk_fma_f32 v[252:253], v[148:149], s[90:91], v[4:5] op_sel_hi:[1,0,1]
	v_med3_f32 v246, v246, s79, v224
	v_med3_f32 v247, v247, s79, v224
	v_med3_f32 v248, v248, s79, v224
	v_med3_f32 v249, v249, s79, v224
	v_med3_f32 v250, v250, s79, v224
	v_med3_f32 v251, v251, s79, v224
	v_med3_f32 v252, v252, s79, v224
	v_med3_f32 v253, v253, s79, v224
	v_fma_f32 v246, v246, 4.0, 4.0
	v_fma_f32 v247, v247, 4.0, 4.0
	v_fma_f32 v248, v248, 4.0, 4.0
	v_fma_f32 v249, v249, 4.0, 4.0
	v_fma_f32 v250, v250, 4.0, 4.0
	v_fma_f32 v251, v251, 4.0, 4.0
	v_fma_f32 v252, v252, 4.0, 4.0
	v_fma_f32 v253, v253, 4.0, 4.0
	v_pk_mul_f32 v[238:239], v[246:247], v[238:239]
	v_pk_mul_f32 v[240:241], v[248:249], v[240:241]
	v_pk_mul_f32 v[242:243], v[250:251], v[242:243]
	v_pk_mul_f32 v[244:245], v[252:253], v[244:245]
	v_or_b32_e32 v26, 32, v22
	v_ashrrev_i32_e32 v27, 31, v26
	v_lshlrev_b64 v[26:27], 11, v[26:27]
	v_lshl_add_u64 v[26:27], s[6:7], 0, v[26:27]
	v_lshl_add_u64 v[26:27], v[26:27], 0, v[20:21]
	v_mov_b32_e32 v24, v201
	v_mov_b32_e32 v25, v201
	v_cvt_pk_fp8_f32 v24, v238, v239
	v_cvt_pk_fp8_f32 v25, v242, v243
	v_cvt_pk_fp8_f32 v24, v240, v241 op_sel:[0,0,1]
	v_cvt_pk_fp8_f32 v25, v244, v245 op_sel:[0,0,1]
	global_store_dwordx2 v[26:27], v[24:25], off
	v_pk_fma_f32 v[238:239], v[142:143], s[90:91], v[14:15] op_sel_hi:[1,0,1]
	v_pk_fma_f32 v[240:241], v[144:145], s[90:91], v[16:17] op_sel_hi:[1,0,1]
	v_pk_fma_f32 v[242:243], v[134:135], s[90:91], v[6:7] op_sel_hi:[1,0,1]
	v_pk_fma_f32 v[244:245], v[136:137], s[90:91], v[8:9] op_sel_hi:[1,0,1]
	v_min_f32_e32 v238, 0x40e00000, v238
	v_min_f32_e32 v239, 0x40e00000, v239
	v_min_f32_e32 v240, 0x40e00000, v240
	v_min_f32_e32 v241, 0x40e00000, v241
	v_min_f32_e32 v242, 0x40e00000, v242
	v_min_f32_e32 v243, 0x40e00000, v243
	v_min_f32_e32 v244, 0x40e00000, v244
	v_min_f32_e32 v245, 0x40e00000, v245
	v_pk_mul_f32 v[246:247], v[238:239], s[92:93] op_sel_hi:[1,0]
	v_pk_mul_f32 v[248:249], v[240:241], s[92:93] op_sel_hi:[1,0]
	v_pk_mul_f32 v[250:251], v[242:243], s[92:93] op_sel_hi:[1,0]
	v_pk_mul_f32 v[252:253], v[244:245], s[92:93] op_sel_hi:[1,0]
	v_exp_f32_e32 v246, v246
	v_exp_f32_e32 v247, v247
	v_exp_f32_e32 v248, v248
	v_exp_f32_e32 v249, v249
	v_exp_f32_e32 v250, v250
	v_exp_f32_e32 v251, v251
	v_exp_f32_e32 v252, v252
	v_exp_f32_e32 v253, v253
	v_pk_add_f32 v[246:247], v[246:247], s[96:97] op_sel_hi:[1,0]
	v_pk_add_f32 v[248:249], v[248:249], s[96:97] op_sel_hi:[1,0]
	v_pk_add_f32 v[250:251], v[250:251], s[96:97] op_sel_hi:[1,0]
	v_pk_add_f32 v[252:253], v[252:253], s[96:97] op_sel_hi:[1,0]
	v_rcp_f32_e32 v246, v246
	v_rcp_f32_e32 v247, v247
	v_rcp_f32_e32 v248, v248
	v_rcp_f32_e32 v249, v249
	v_rcp_f32_e32 v250, v250
	v_rcp_f32_e32 v251, v251
	v_rcp_f32_e32 v252, v252
	v_rcp_f32_e32 v253, v253
	v_pk_mul_f32 v[238:239], v[238:239], v[246:247]
	v_pk_mul_f32 v[240:241], v[240:241], v[248:249]
	v_pk_mul_f32 v[242:243], v[242:243], v[250:251]
	v_pk_mul_f32 v[244:245], v[244:245], v[252:253]
	v_pk_fma_f32 v[246:247], v[138:139], s[90:91], v[10:11] op_sel_hi:[1,0,1]
	v_pk_fma_f32 v[248:249], v[140:141], s[90:91], v[12:13] op_sel_hi:[1,0,1]
	v_pk_fma_f32 v[250:251], v[130:131], s[90:91], v[2:3] op_sel_hi:[1,0,1]
	v_pk_fma_f32 v[252:253], v[132:133], s[90:91], v[4:5] op_sel_hi:[1,0,1]
	v_med3_f32 v246, v246, s79, v224
	v_med3_f32 v247, v247, s79, v224
	v_med3_f32 v248, v248, s79, v224
	v_med3_f32 v249, v249, s79, v224
	v_med3_f32 v250, v250, s79, v224
	v_med3_f32 v251, v251, s79, v224
	v_med3_f32 v252, v252, s79, v224
	v_med3_f32 v253, v253, s79, v224
	v_fma_f32 v246, v246, 4.0, 4.0
	v_fma_f32 v247, v247, 4.0, 4.0
	v_fma_f32 v248, v248, 4.0, 4.0
	v_fma_f32 v249, v249, 4.0, 4.0
	v_fma_f32 v250, v250, 4.0, 4.0
	v_fma_f32 v251, v251, 4.0, 4.0
	v_fma_f32 v252, v252, 4.0, 4.0
	v_fma_f32 v253, v253, 4.0, 4.0
	v_pk_mul_f32 v[238:239], v[246:247], v[238:239]
	v_pk_mul_f32 v[240:241], v[248:249], v[240:241]
	v_pk_mul_f32 v[242:243], v[250:251], v[242:243]
	v_pk_mul_f32 v[244:245], v[252:253], v[244:245]
	v_or_b32_e32 v22, 48, v22
	v_ashrrev_i32_e32 v23, 31, v22
	v_lshlrev_b64 v[22:23], 11, v[22:23]
	v_lshl_add_u64 v[22:23], s[6:7], 0, v[22:23]
	v_lshl_add_u64 v[20:21], v[22:23], 0, v[20:21]
	v_mov_b32_e32 v24, v201
	v_mov_b32_e32 v25, v201
	v_cvt_pk_fp8_f32 v24, v238, v239
	v_cvt_pk_fp8_f32 v25, v242, v243
	v_cvt_pk_fp8_f32 v24, v240, v241 op_sel:[0,0,1]
	v_cvt_pk_fp8_f32 v25, v244, v245 op_sel:[0,0,1]
	global_store_dwordx2 v[20:21], v[24:25], off
	v_pk_fma_f32 v[238:239], v[126:127], s[90:91], v[14:15] op_sel_hi:[1,0,1]
	v_pk_fma_f32 v[240:241], v[128:129], s[90:91], v[16:17] op_sel_hi:[1,0,1]
	v_pk_fma_f32 v[242:243], v[118:119], s[90:91], v[6:7] op_sel_hi:[1,0,1]
	v_pk_fma_f32 v[244:245], v[120:121], s[90:91], v[8:9] op_sel_hi:[1,0,1]
	v_min_f32_e32 v238, 0x40e00000, v238
	v_min_f32_e32 v239, 0x40e00000, v239
	v_min_f32_e32 v240, 0x40e00000, v240
	v_min_f32_e32 v241, 0x40e00000, v241
	v_min_f32_e32 v242, 0x40e00000, v242
	v_min_f32_e32 v243, 0x40e00000, v243
	v_min_f32_e32 v244, 0x40e00000, v244
	v_min_f32_e32 v245, 0x40e00000, v245
	v_pk_mul_f32 v[246:247], v[238:239], s[92:93] op_sel_hi:[1,0]
	v_pk_mul_f32 v[248:249], v[240:241], s[92:93] op_sel_hi:[1,0]
	v_pk_mul_f32 v[250:251], v[242:243], s[92:93] op_sel_hi:[1,0]
	v_pk_mul_f32 v[252:253], v[244:245], s[92:93] op_sel_hi:[1,0]
	v_exp_f32_e32 v246, v246
	v_exp_f32_e32 v247, v247
	v_exp_f32_e32 v248, v248
	v_exp_f32_e32 v249, v249
	v_exp_f32_e32 v250, v250
	v_exp_f32_e32 v251, v251
	v_exp_f32_e32 v252, v252
	v_exp_f32_e32 v253, v253
	v_pk_add_f32 v[246:247], v[246:247], s[96:97] op_sel_hi:[1,0]
	v_pk_add_f32 v[248:249], v[248:249], s[96:97] op_sel_hi:[1,0]
	v_pk_add_f32 v[250:251], v[250:251], s[96:97] op_sel_hi:[1,0]
	v_pk_add_f32 v[252:253], v[252:253], s[96:97] op_sel_hi:[1,0]
	v_rcp_f32_e32 v246, v246
	v_rcp_f32_e32 v247, v247
	v_rcp_f32_e32 v248, v248
	v_rcp_f32_e32 v249, v249
	v_rcp_f32_e32 v250, v250
	v_rcp_f32_e32 v251, v251
	v_rcp_f32_e32 v252, v252
	v_rcp_f32_e32 v253, v253
	v_pk_mul_f32 v[238:239], v[238:239], v[246:247]
	v_pk_mul_f32 v[240:241], v[240:241], v[248:249]
	v_pk_mul_f32 v[242:243], v[242:243], v[250:251]
	v_pk_mul_f32 v[244:245], v[244:245], v[252:253]
	v_pk_fma_f32 v[246:247], v[122:123], s[90:91], v[10:11] op_sel_hi:[1,0,1]
	v_pk_fma_f32 v[248:249], v[124:125], s[90:91], v[12:13] op_sel_hi:[1,0,1]
	v_pk_fma_f32 v[250:251], v[114:115], s[90:91], v[2:3] op_sel_hi:[1,0,1]
	v_pk_fma_f32 v[252:253], v[116:117], s[90:91], v[4:5] op_sel_hi:[1,0,1]
	v_med3_f32 v246, v246, s79, v224
	v_med3_f32 v247, v247, s79, v224
	v_med3_f32 v248, v248, s79, v224
	v_med3_f32 v249, v249, s79, v224
	v_med3_f32 v250, v250, s79, v224
	v_med3_f32 v251, v251, s79, v224
	v_med3_f32 v252, v252, s79, v224
	v_med3_f32 v253, v253, s79, v224
	v_fma_f32 v246, v246, 4.0, 4.0
	v_fma_f32 v247, v247, 4.0, 4.0
	v_fma_f32 v248, v248, 4.0, 4.0
	v_fma_f32 v249, v249, 4.0, 4.0
	v_fma_f32 v250, v250, 4.0, 4.0
	v_fma_f32 v251, v251, 4.0, 4.0
	v_fma_f32 v252, v252, 4.0, 4.0
	v_fma_f32 v253, v253, 4.0, 4.0
	v_pk_mul_f32 v[238:239], v[246:247], v[238:239]
	v_pk_mul_f32 v[240:241], v[248:249], v[240:241]
	v_pk_mul_f32 v[242:243], v[250:251], v[242:243]
	v_pk_mul_f32 v[244:245], v[252:253], v[244:245]
	v_add_co_u32_e32 v22, vcc, s80, v18
	s_nop 0
	v_addc_co_u32_e32 v23, vcc, 0, v19, vcc
	v_mov_b32_e32 v20, v201
	v_mov_b32_e32 v21, v201
	v_cvt_pk_fp8_f32 v20, v238, v239
	v_cvt_pk_fp8_f32 v21, v242, v243
	v_cvt_pk_fp8_f32 v20, v240, v241 op_sel:[0,0,1]
	v_cvt_pk_fp8_f32 v21, v244, v245 op_sel:[0,0,1]
	global_store_dwordx2 v[22:23], v[20:21], off
	v_pk_fma_f32 v[238:239], v[110:111], s[90:91], v[14:15] op_sel_hi:[1,0,1]
	v_pk_fma_f32 v[240:241], v[112:113], s[90:91], v[16:17] op_sel_hi:[1,0,1]
	v_pk_fma_f32 v[242:243], v[102:103], s[90:91], v[6:7] op_sel_hi:[1,0,1]
	v_pk_fma_f32 v[244:245], v[104:105], s[90:91], v[8:9] op_sel_hi:[1,0,1]
	v_min_f32_e32 v238, 0x40e00000, v238
	v_min_f32_e32 v239, 0x40e00000, v239
	v_min_f32_e32 v240, 0x40e00000, v240
	v_min_f32_e32 v241, 0x40e00000, v241
	v_min_f32_e32 v242, 0x40e00000, v242
	v_min_f32_e32 v243, 0x40e00000, v243
	v_min_f32_e32 v244, 0x40e00000, v244
	v_min_f32_e32 v245, 0x40e00000, v245
	v_pk_mul_f32 v[246:247], v[238:239], s[92:93] op_sel_hi:[1,0]
	v_pk_mul_f32 v[248:249], v[240:241], s[92:93] op_sel_hi:[1,0]
	v_pk_mul_f32 v[250:251], v[242:243], s[92:93] op_sel_hi:[1,0]
	v_pk_mul_f32 v[252:253], v[244:245], s[92:93] op_sel_hi:[1,0]
	v_exp_f32_e32 v246, v246
	v_exp_f32_e32 v247, v247
	v_exp_f32_e32 v248, v248
	v_exp_f32_e32 v249, v249
	v_exp_f32_e32 v250, v250
	v_exp_f32_e32 v251, v251
	v_exp_f32_e32 v252, v252
	v_exp_f32_e32 v253, v253
	v_pk_add_f32 v[246:247], v[246:247], s[96:97] op_sel_hi:[1,0]
	v_pk_add_f32 v[248:249], v[248:249], s[96:97] op_sel_hi:[1,0]
	v_pk_add_f32 v[250:251], v[250:251], s[96:97] op_sel_hi:[1,0]
	v_pk_add_f32 v[252:253], v[252:253], s[96:97] op_sel_hi:[1,0]
	v_rcp_f32_e32 v246, v246
	v_rcp_f32_e32 v247, v247
	v_rcp_f32_e32 v248, v248
	v_rcp_f32_e32 v249, v249
	v_rcp_f32_e32 v250, v250
	v_rcp_f32_e32 v251, v251
	v_rcp_f32_e32 v252, v252
	v_rcp_f32_e32 v253, v253
	v_pk_mul_f32 v[238:239], v[238:239], v[246:247]
	v_pk_mul_f32 v[240:241], v[240:241], v[248:249]
	v_pk_mul_f32 v[242:243], v[242:243], v[250:251]
	v_pk_mul_f32 v[244:245], v[244:245], v[252:253]
	v_pk_fma_f32 v[246:247], v[106:107], s[90:91], v[10:11] op_sel_hi:[1,0,1]
	v_pk_fma_f32 v[248:249], v[108:109], s[90:91], v[12:13] op_sel_hi:[1,0,1]
	v_pk_fma_f32 v[250:251], v[98:99], s[90:91], v[2:3] op_sel_hi:[1,0,1]
	v_pk_fma_f32 v[252:253], v[100:101], s[90:91], v[4:5] op_sel_hi:[1,0,1]
	v_med3_f32 v246, v246, s79, v224
	v_med3_f32 v247, v247, s79, v224
	v_med3_f32 v248, v248, s79, v224
	v_med3_f32 v249, v249, s79, v224
	v_med3_f32 v250, v250, s79, v224
	v_med3_f32 v251, v251, s79, v224
	v_med3_f32 v252, v252, s79, v224
	v_med3_f32 v253, v253, s79, v224
	v_fma_f32 v246, v246, 4.0, 4.0
	v_fma_f32 v247, v247, 4.0, 4.0
	v_fma_f32 v248, v248, 4.0, 4.0
	v_fma_f32 v249, v249, 4.0, 4.0
	v_fma_f32 v250, v250, 4.0, 4.0
	v_fma_f32 v251, v251, 4.0, 4.0
	v_fma_f32 v252, v252, 4.0, 4.0
	v_fma_f32 v253, v253, 4.0, 4.0
	v_pk_mul_f32 v[238:239], v[246:247], v[238:239]
	v_pk_mul_f32 v[240:241], v[248:249], v[240:241]
	v_pk_mul_f32 v[242:243], v[250:251], v[242:243]
	v_pk_mul_f32 v[244:245], v[252:253], v[244:245]
	v_add_co_u32_e32 v22, vcc, s81, v18
	s_nop 0
	v_addc_co_u32_e32 v23, vcc, 0, v19, vcc
	v_mov_b32_e32 v20, v201
	v_mov_b32_e32 v21, v201
	v_cvt_pk_fp8_f32 v20, v238, v239
	v_cvt_pk_fp8_f32 v21, v242, v243
	v_cvt_pk_fp8_f32 v20, v240, v241 op_sel:[0,0,1]
	v_cvt_pk_fp8_f32 v21, v244, v245 op_sel:[0,0,1]
	global_store_dwordx2 v[22:23], v[20:21], off
	v_pk_fma_f32 v[238:239], v[94:95], s[90:91], v[14:15] op_sel_hi:[1,0,1]
	v_pk_fma_f32 v[240:241], v[96:97], s[90:91], v[16:17] op_sel_hi:[1,0,1]
	v_pk_fma_f32 v[242:243], v[86:87], s[90:91], v[6:7] op_sel_hi:[1,0,1]
	v_pk_fma_f32 v[244:245], v[88:89], s[90:91], v[8:9] op_sel_hi:[1,0,1]
	v_min_f32_e32 v238, 0x40e00000, v238
	v_min_f32_e32 v239, 0x40e00000, v239
	v_min_f32_e32 v240, 0x40e00000, v240
	v_min_f32_e32 v241, 0x40e00000, v241
	v_min_f32_e32 v242, 0x40e00000, v242
	v_min_f32_e32 v243, 0x40e00000, v243
	v_min_f32_e32 v244, 0x40e00000, v244
	v_min_f32_e32 v245, 0x40e00000, v245
	v_pk_mul_f32 v[246:247], v[238:239], s[92:93] op_sel_hi:[1,0]
	v_pk_mul_f32 v[248:249], v[240:241], s[92:93] op_sel_hi:[1,0]
	v_pk_mul_f32 v[250:251], v[242:243], s[92:93] op_sel_hi:[1,0]
	v_pk_mul_f32 v[252:253], v[244:245], s[92:93] op_sel_hi:[1,0]
	v_exp_f32_e32 v246, v246
	v_exp_f32_e32 v247, v247
	v_exp_f32_e32 v248, v248
	v_exp_f32_e32 v249, v249
	v_exp_f32_e32 v250, v250
	v_exp_f32_e32 v251, v251
	v_exp_f32_e32 v252, v252
	v_exp_f32_e32 v253, v253
	v_pk_add_f32 v[246:247], v[246:247], s[96:97] op_sel_hi:[1,0]
	v_pk_add_f32 v[248:249], v[248:249], s[96:97] op_sel_hi:[1,0]
	v_pk_add_f32 v[250:251], v[250:251], s[96:97] op_sel_hi:[1,0]
	v_pk_add_f32 v[252:253], v[252:253], s[96:97] op_sel_hi:[1,0]
	v_rcp_f32_e32 v246, v246
	v_rcp_f32_e32 v247, v247
	v_rcp_f32_e32 v248, v248
	v_rcp_f32_e32 v249, v249
	v_rcp_f32_e32 v250, v250
	v_rcp_f32_e32 v251, v251
	v_rcp_f32_e32 v252, v252
	v_rcp_f32_e32 v253, v253
	v_pk_mul_f32 v[238:239], v[238:239], v[246:247]
	v_pk_mul_f32 v[240:241], v[240:241], v[248:249]
	v_pk_mul_f32 v[242:243], v[242:243], v[250:251]
	v_pk_mul_f32 v[244:245], v[244:245], v[252:253]
	v_pk_fma_f32 v[246:247], v[90:91], s[90:91], v[10:11] op_sel_hi:[1,0,1]
	v_pk_fma_f32 v[248:249], v[92:93], s[90:91], v[12:13] op_sel_hi:[1,0,1]
	v_pk_fma_f32 v[250:251], v[82:83], s[90:91], v[2:3] op_sel_hi:[1,0,1]
	v_pk_fma_f32 v[252:253], v[84:85], s[90:91], v[4:5] op_sel_hi:[1,0,1]
	v_med3_f32 v246, v246, s79, v224
	v_med3_f32 v247, v247, s79, v224
	v_med3_f32 v248, v248, s79, v224
	v_med3_f32 v249, v249, s79, v224
	v_med3_f32 v250, v250, s79, v224
	v_med3_f32 v251, v251, s79, v224
	v_med3_f32 v252, v252, s79, v224
	v_med3_f32 v253, v253, s79, v224
	v_fma_f32 v246, v246, 4.0, 4.0
	v_fma_f32 v247, v247, 4.0, 4.0
	v_fma_f32 v248, v248, 4.0, 4.0
	v_fma_f32 v249, v249, 4.0, 4.0
	v_fma_f32 v250, v250, 4.0, 4.0
	v_fma_f32 v251, v251, 4.0, 4.0
	v_fma_f32 v252, v252, 4.0, 4.0
	v_fma_f32 v253, v253, 4.0, 4.0
	v_pk_mul_f32 v[238:239], v[246:247], v[238:239]
	v_pk_mul_f32 v[240:241], v[248:249], v[240:241]
	v_pk_mul_f32 v[242:243], v[250:251], v[242:243]
	v_pk_mul_f32 v[244:245], v[252:253], v[244:245]
	v_add_co_u32_e32 v22, vcc, s82, v18
	s_nop 0
	v_addc_co_u32_e32 v23, vcc, 0, v19, vcc
	v_mov_b32_e32 v20, v201
	v_mov_b32_e32 v21, v201
	v_cvt_pk_fp8_f32 v20, v238, v239
	v_cvt_pk_fp8_f32 v21, v242, v243
	v_cvt_pk_fp8_f32 v20, v240, v241 op_sel:[0,0,1]
	v_cvt_pk_fp8_f32 v21, v244, v245 op_sel:[0,0,1]
	global_store_dwordx2 v[22:23], v[20:21], off
	v_pk_fma_f32 v[238:239], v[78:79], s[90:91], v[14:15] op_sel_hi:[1,0,1]
	v_pk_fma_f32 v[240:241], v[80:81], s[90:91], v[16:17] op_sel_hi:[1,0,1]
	v_pk_fma_f32 v[242:243], v[70:71], s[90:91], v[6:7] op_sel_hi:[1,0,1]
	v_pk_fma_f32 v[244:245], v[72:73], s[90:91], v[8:9] op_sel_hi:[1,0,1]
	v_min_f32_e32 v238, 0x40e00000, v238
	v_min_f32_e32 v239, 0x40e00000, v239
	v_min_f32_e32 v240, 0x40e00000, v240
	v_min_f32_e32 v241, 0x40e00000, v241
	v_min_f32_e32 v242, 0x40e00000, v242
	v_min_f32_e32 v243, 0x40e00000, v243
	v_min_f32_e32 v244, 0x40e00000, v244
	v_min_f32_e32 v245, 0x40e00000, v245
	v_pk_mul_f32 v[246:247], v[238:239], s[92:93] op_sel_hi:[1,0]
	v_pk_mul_f32 v[248:249], v[240:241], s[92:93] op_sel_hi:[1,0]
	v_pk_mul_f32 v[250:251], v[242:243], s[92:93] op_sel_hi:[1,0]
	v_pk_mul_f32 v[252:253], v[244:245], s[92:93] op_sel_hi:[1,0]
	v_exp_f32_e32 v246, v246
	v_exp_f32_e32 v247, v247
	v_exp_f32_e32 v248, v248
	v_exp_f32_e32 v249, v249
	v_exp_f32_e32 v250, v250
	v_exp_f32_e32 v251, v251
	v_exp_f32_e32 v252, v252
	v_exp_f32_e32 v253, v253
	v_pk_add_f32 v[246:247], v[246:247], s[96:97] op_sel_hi:[1,0]
	v_pk_add_f32 v[248:249], v[248:249], s[96:97] op_sel_hi:[1,0]
	v_pk_add_f32 v[250:251], v[250:251], s[96:97] op_sel_hi:[1,0]
	v_pk_add_f32 v[252:253], v[252:253], s[96:97] op_sel_hi:[1,0]
	v_rcp_f32_e32 v246, v246
	v_rcp_f32_e32 v247, v247
	v_rcp_f32_e32 v248, v248
	v_rcp_f32_e32 v249, v249
	v_rcp_f32_e32 v250, v250
	v_rcp_f32_e32 v251, v251
	v_rcp_f32_e32 v252, v252
	v_rcp_f32_e32 v253, v253
	v_pk_mul_f32 v[238:239], v[238:239], v[246:247]
	v_pk_mul_f32 v[240:241], v[240:241], v[248:249]
	v_pk_mul_f32 v[242:243], v[242:243], v[250:251]
	v_pk_mul_f32 v[244:245], v[244:245], v[252:253]
	v_pk_fma_f32 v[246:247], v[74:75], s[90:91], v[10:11] op_sel_hi:[1,0,1]
	v_pk_fma_f32 v[248:249], v[76:77], s[90:91], v[12:13] op_sel_hi:[1,0,1]
	v_pk_fma_f32 v[250:251], v[66:67], s[90:91], v[2:3] op_sel_hi:[1,0,1]
	v_pk_fma_f32 v[252:253], v[68:69], s[90:91], v[4:5] op_sel_hi:[1,0,1]
	v_med3_f32 v246, v246, s79, v224
	v_med3_f32 v247, v247, s79, v224
	v_med3_f32 v248, v248, s79, v224
	v_med3_f32 v249, v249, s79, v224
	v_med3_f32 v250, v250, s79, v224
	v_med3_f32 v251, v251, s79, v224
	v_med3_f32 v252, v252, s79, v224
	v_med3_f32 v253, v253, s79, v224
	v_fma_f32 v246, v246, 4.0, 4.0
	v_fma_f32 v247, v247, 4.0, 4.0
	v_fma_f32 v248, v248, 4.0, 4.0
	v_fma_f32 v249, v249, 4.0, 4.0
	v_fma_f32 v250, v250, 4.0, 4.0
	v_fma_f32 v251, v251, 4.0, 4.0
	v_fma_f32 v252, v252, 4.0, 4.0
	v_fma_f32 v253, v253, 4.0, 4.0
	v_pk_mul_f32 v[238:239], v[246:247], v[238:239]
	v_pk_mul_f32 v[240:241], v[248:249], v[240:241]
	v_pk_mul_f32 v[242:243], v[250:251], v[242:243]
	v_pk_mul_f32 v[244:245], v[252:253], v[244:245]
	v_add_co_u32_e32 v4, vcc, 0x58000, v18
	s_nop 1
	v_addc_co_u32_e32 v5, vcc, 0, v19, vcc
	s_and_b64 vcc, exec, s[4:5]
	s_mov_b64 s[4:5], -1
	v_mov_b32_e32 v2, v201
	v_mov_b32_e32 v3, v201
	v_cvt_pk_fp8_f32 v2, v238, v239
	v_cvt_pk_fp8_f32 v3, v242, v243
	v_cvt_pk_fp8_f32 v2, v240, v241 op_sel:[0,0,1]
	v_cvt_pk_fp8_f32 v3, v244, v245 op_sel:[0,0,1]
	global_store_dwordx2 v[4:5], v[2:3], off
	s_cbranch_vccnz .LBB0_2061
	s_andn2_b64 vcc, exec, s[20:21]
	s_cbranch_vccnz .LBB0_2060
	s_barrier
	s_branch .LBB0_2060
